# attention epilogue: v_permlane32_swap pairs 8-byte output pieces into 16-byte dwordx4 stores (4 stores per lane instead of 8)
# baseline (speedup 1.0000x reference)
.LBB2_24:
	v_min_u32_e32 v2, s14, v220
	s_waitcnt lgkmcnt(0)
	v_mul_hi_u32 v3, v2, v217
	v_mul_lo_u32 v4, v3, s3
	v_sub_u32_e32 v4, v2, v4
	v_add_u32_e32 v5, 1, v3
	v_cmp_le_u32_e32 vcc, s3, v4
	s_nop 1
	v_cndmask_b32_e32 v3, v3, v5, vcc
	v_subrev_u32_e32 v5, s3, v4
	v_cndmask_b32_e32 v4, v4, v5, vcc
	v_add_u32_e32 v5, 1, v3
	v_cmp_le_u32_e32 vcc, s3, v4
	s_nop 1
	v_cndmask_b32_e32 v225, v3, v5, vcc
	v_mul_lo_u32 v3, v225, s3
	v_sub_u32_e32 v226, v2, v3
	v_mul_lo_u32 v2, v225, 14
	v_add_lshl_u32 v2, v226, v2, 6
	v_ashrrev_i32_e32 v3, 31, v2
	v_lshl_add_u64 v[34:35], v[2:3], 1, v[212:213]
	global_load_dwordx4 v[198:201], v[34:35], off
	global_load_dwordx4 v[186:189], v[34:35], off offset:32
	global_load_dwordx4 v[194:197], v[34:35], off offset:64
	global_load_dwordx4 v[190:193], v[34:35], off offset:96
	v_add_u32_e32 v34, 0xe000, v215
	v_add_u32_e32 v35, v218, v214
	v_lshl_add_u32 v36, v225, 1, v216
	v_lshl_add_u32 v37, v226, 1, v216
	s_waitcnt vmcnt(3)
	v_mfma_f32_32x32x16_f16 v[18:33], v[146:149], v[198:201], 0
	v_mfma_f32_32x32x16_f16 v[2:17], v[170:173], v[198:201], 0
	s_waitcnt vmcnt(2)
	v_mfma_f32_32x32x16_f16 v[18:33], v[150:153], v[186:189], v[18:33]
	v_mfma_f32_32x32x16_f16 v[2:17], v[162:165], v[186:189], v[2:17]
	s_waitcnt vmcnt(1)
	v_mfma_f32_32x32x16_f16 v[18:33], v[154:157], v[194:197], v[18:33]
	v_mfma_f32_32x32x16_f16 v[2:17], v[166:169], v[194:197], v[2:17]
	s_waitcnt vmcnt(0)
	v_mfma_f32_32x32x16_f16 v[18:33], v[158:161], v[190:193], v[18:33]
	v_mfma_f32_32x32x16_f16 v[2:17], v[174:177], v[190:193], v[2:17]
	s_nop 10
	v_cvt_pk_f16_f32 v18, v18, v19
	v_cvt_pk_f16_f32 v19, v20, v21
	v_cvt_pk_f16_f32 v2, v2, v3
	v_cvt_pk_f16_f32 v3, v4, v5
	v_cvt_pk_f16_f32 v4, v22, v23
	v_cvt_pk_f16_f32 v5, v24, v25
	v_cvt_pk_f16_f32 v6, v6, v7
	v_cvt_pk_f16_f32 v7, v8, v9
	v_cvt_pk_f16_f32 v8, v26, v27
	v_cvt_pk_f16_f32 v9, v28, v29
	v_cvt_pk_f16_f32 v10, v10, v11
	v_cvt_pk_f16_f32 v11, v12, v13
	v_cvt_pk_f16_f32 v12, v30, v31
	v_cvt_pk_f16_f32 v13, v32, v33
	v_cvt_pk_f16_f32 v14, v14, v15
	v_cvt_pk_f16_f32 v15, v16, v17
	ds_write2_b64 v34, v[18:19], v[4:5] offset0:72 offset1:74
	ds_write2_b64 v34, v[2:3], v[6:7] offset0:80 offset1:82
	ds_write2_b64 v34, v[8:9], v[12:13] offset0:76 offset1:78
	ds_write2_b64 v34, v[10:11], v[14:15] offset0:84 offset1:86
	s_waitcnt lgkmcnt(0)
	ds_read_b128 v[206:209], v36 offset:57920
	ds_read_b128 v[202:205], v37 offset:57974
	s_waitcnt lgkmcnt(0)
	ds_read_b128 v[2:5], v35
	ds_read_b128 v[6:9], v35 offset:32
	s_waitcnt lgkmcnt(1)
	v_mfma_f32_32x32x16_f16 v[82:97], v[2:5], v[198:201], 0
	ds_read_b128 v[2:5], v221
	ds_read_b128 v[10:13], v221 offset:32
	s_waitcnt lgkmcnt(1)
	v_mfma_f32_32x32x16_f16 v[66:81], v[2:5], v[198:201], 0
	ds_read_b128 v[2:5], v221 offset:4608
	ds_read_b128 v[14:17], v221 offset:4640
	v_mfma_f32_32x32x16_f16 v[82:97], v[6:9], v[186:189], v[82:97]
	s_waitcnt lgkmcnt(1)
	v_mfma_f32_32x32x16_f16 v[50:65], v[2:5], v[198:201], 0
	ds_read_b128 v[2:5], v35 offset:64
	ds_read_b128 v[6:9], v35 offset:96
	v_mfma_f32_32x32x16_f16 v[66:81], v[10:13], v[186:189], v[66:81]
	s_waitcnt lgkmcnt(1)
	v_mfma_f32_32x32x16_f16 v[82:97], v[2:5], v[194:197], v[82:97]
	ds_read_b128 v[2:5], v221 offset:64
	ds_read_b128 v[10:13], v221 offset:96
	v_mfma_f32_32x32x16_f16 v[50:65], v[14:17], v[186:189], v[50:65]
	s_waitcnt lgkmcnt(1)
	v_mfma_f32_32x32x16_f16 v[66:81], v[2:5], v[194:197], v[66:81]
	v_mfma_f32_32x32x16_f16 v[82:97], v[6:9], v[190:193], v[82:97]
	ds_read_b128 v[2:5], v221 offset:4672
	ds_read_b128 v[6:9], v221 offset:4704
	s_waitcnt lgkmcnt(1)
	v_mfma_f32_32x32x16_f16 v[50:65], v[2:5], v[194:197], v[50:65]
	s_waitcnt lgkmcnt(0)
	v_mfma_f32_32x32x16_f16 v[50:65], v[6:9], v[190:193], v[50:65]
	ds_read_b128 v[2:5], v221 offset:9216
	ds_read_b128 v[6:9], v221 offset:9248
	s_waitcnt lgkmcnt(1)
	v_mfma_f32_32x32x16_f16 v[34:49], v[2:5], v[198:201], 0
	s_waitcnt lgkmcnt(0)
	v_mfma_f32_32x32x16_f16 v[34:49], v[6:9], v[186:189], v[34:49]
	ds_read_b128 v[2:5], v221 offset:9280
	ds_read_b128 v[6:9], v221 offset:9312
	s_waitcnt lgkmcnt(1)
	v_mfma_f32_32x32x16_f16 v[34:49], v[2:5], v[194:197], v[34:49]
	s_waitcnt lgkmcnt(0)
	v_mfma_f32_32x32x16_f16 v[34:49], v[6:9], v[190:193], v[34:49]
	ds_read_b128 v[2:5], v221 offset:13824
	ds_read_b128 v[6:9], v221 offset:13856
	s_waitcnt lgkmcnt(1)
	v_mfma_f32_32x32x16_f16 v[18:33], v[2:5], v[198:201], 0
	s_waitcnt lgkmcnt(0)
	v_mfma_f32_32x32x16_f16 v[18:33], v[6:9], v[186:189], v[18:33]
	ds_read_b128 v[2:5], v221 offset:13888
	ds_read_b128 v[6:9], v221 offset:13920
	s_waitcnt lgkmcnt(1)
	v_mfma_f32_32x32x16_f16 v[18:33], v[2:5], v[194:197], v[18:33]
	ds_read_b128 v[2:5], v221 offset:23040
	ds_read_b128 v[228:231], v221 offset:23072
	v_mfma_f32_32x32x16_f16 v[66:81], v[10:13], v[190:193], v[66:81]
	s_waitcnt lgkmcnt(2)
	v_mfma_f32_32x32x16_f16 v[18:33], v[6:9], v[190:193], v[18:33]
	s_waitcnt lgkmcnt(1)
	v_mfma_f32_32x32x16_f16 v[2:17], v[2:5], v[198:201], 0
	s_waitcnt lgkmcnt(0)
	v_mfma_f32_32x32x16_f16 v[2:17], v[228:231], v[186:189], v[2:17]
	ds_read_b128 v[228:231], v221 offset:23104
	ds_read_b128 v[232:235], v221 offset:23136
	s_waitcnt lgkmcnt(1)
	v_mfma_f32_32x32x16_f16 v[2:17], v[228:231], v[194:197], v[2:17]
	s_waitcnt lgkmcnt(0)
	v_mfma_f32_32x32x16_f16 v[2:17], v[232:235], v[190:193], v[2:17]
	v_mfma_f32_32x32x16_f16 v[82:97], v[102:105], v[206:209], v[82:97]
	v_mfma_f32_32x32x16_f16 v[2:17], v[98:101], v[206:209], v[2:17]
	v_mfma_f32_32x32x16_f16 v[82:97], v[106:109], v[202:205], v[82:97]
	v_mfma_f32_32x32x16_f16 v[2:17], v[182:185], v[202:205], v[2:17]
	s_nop 11
	ds_read_b128 v[6:9], v221 offset:18432
	ds_read_b128 v[232:235], v221 offset:18464
	ds_read_b128 v[236:239], v221 offset:18496
	ds_read_b128 v[240:243], v221 offset:18528
	v_cndmask_b32_e64 v230, v223, v2, s[4:5]
	v_max_f32_e32 v2, v82, v82
	v_max_f32_e32 v2, 0xf149f2ca, v2
	v_max3_f32 v2, v2, v83, v84
	v_max3_f32 v2, v2, v85, v86
	v_max3_f32 v2, v2, v87, v88
	v_mfma_f32_32x32x16_f16 v[66:81], v[110:113], v[206:209], v[66:81]
	v_cndmask_b32_e64 v227, v223, v5, s[4:5]
	v_cndmask_b32_e64 v228, v223, v4, s[4:5]
	v_cndmask_b32_e64 v229, v223, v3, s[4:5]
	v_max3_f32 v231, v2, v89, v90
	s_waitcnt lgkmcnt(3)
	v_mfma_f32_32x32x16_f16 v[2:17], v[6:9], v[198:201], 0
	v_max3_f32 v198, v231, v91, v92
	v_max3_f32 v198, v198, v93, v94
	v_max3_f32 v198, v198, v95, v96
	v_mfma_f32_32x32x16_f16 v[66:81], v[114:117], v[202:205], v[66:81]
	v_mfma_f32_32x32x16_f16 v[50:65], v[118:121], v[206:209], v[50:65]
	s_nop 10
	v_max3_f32 v198, v198, v97, v66
	v_max3_f32 v198, v198, v67, v68
	v_max3_f32 v198, v198, v69, v70
	v_max3_f32 v198, v198, v71, v72
	s_waitcnt lgkmcnt(2)
	v_mfma_f32_32x32x16_f16 v[2:17], v[232:235], v[186:189], v[2:17]
	v_max3_f32 v186, v198, v73, v74
	v_max3_f32 v186, v186, v75, v76
	v_max3_f32 v186, v186, v77, v78
	v_max3_f32 v186, v186, v79, v80
	v_and_b32_e32 v188, 64, v222
	v_xor_b32_e32 v187, 32, v222
	v_add_u32_e32 v188, 64, v188
	v_mfma_f32_32x32x16_f16 v[50:65], v[122:125], v[202:205], v[50:65]
	v_cmp_lt_i32_e32 vcc, v187, v188
	s_nop 1
	v_cndmask_b32_e32 v187, v222, v187, vcc
	v_cmp_gt_u32_e32 vcc, s12, v220
	s_nop 6
	v_max3_f32 v186, v186, v81, v50
	v_mfma_f32_32x32x16_f16 v[34:49], v[126:129], v[206:209], v[34:49]
	v_max3_f32 v186, v186, v51, v52
	v_max3_f32 v186, v186, v53, v54
	v_max3_f32 v186, v186, v55, v56
	v_max3_f32 v186, v186, v57, v58
	v_max3_f32 v186, v186, v59, v60
	v_max3_f32 v186, v186, v61, v62
	v_max3_f32 v186, v186, v63, v64
	s_waitcnt lgkmcnt(1)
	v_mfma_f32_32x32x16_f16 v[2:17], v[236:239], v[194:197], v[2:17]
	v_lshlrev_b32_e32 v194, 2, v187
	v_mfma_f32_32x32x16_f16 v[34:49], v[130:133], v[202:205], v[34:49]
	v_mfma_f32_32x32x16_f16 v[18:33], v[134:137], v[206:209], v[18:33]
	s_nop 10
	v_max3_f32 v186, v186, v65, v34
	v_max3_f32 v186, v186, v35, v36
	v_max3_f32 v186, v186, v37, v38
	v_max3_f32 v186, v186, v39, v40
	v_max3_f32 v186, v186, v41, v42
	v_max3_f32 v186, v186, v43, v44
	v_max3_f32 v186, v186, v45, v46
	s_waitcnt lgkmcnt(0)
	v_mfma_f32_32x32x16_f16 v[2:17], v[240:243], v[190:193], v[2:17]
	v_max3_f32 v186, v186, v47, v48
	v_mfma_f32_32x32x16_f16 v[18:33], v[138:141], v[202:205], v[18:33]
	v_mfma_f32_32x32x16_f16 v[2:17], v[142:145], v[206:209], v[2:17]
	s_nop 10
	v_max3_f32 v186, v186, v49, v18
	v_max3_f32 v186, v186, v19, v20
	v_max3_f32 v186, v186, v21, v22
	v_max3_f32 v186, v186, v23, v24
	v_max3_f32 v186, v186, v25, v26
	v_max3_f32 v186, v186, v27, v28
	v_max3_f32 v186, v186, v29, v30
	v_mfma_f32_32x32x16_f16 v[2:17], v[178:181], v[202:205], v[2:17]
	v_max3_f32 v186, v186, v31, v32
	s_nop 10
	v_max3_f32 v186, v186, v33, v2
	v_max3_f32 v186, v186, v3, v4
	v_max3_f32 v186, v186, v5, v6
	v_max3_f32 v186, v186, v7, v8
	v_max3_f32 v186, v186, v9, v10
	v_max3_f32 v186, v186, v11, v12
	v_max3_f32 v186, v186, v13, v14
	v_max3_f32 v186, v186, v15, v16
	v_max3_f32 v186, v186, v17, v230
	v_max3_f32 v186, v186, v229, v228
	v_max3_f32 v186, v186, v227, s17
	ds_bpermute_b32 v187, v194, v186
	s_waitcnt lgkmcnt(0)
	v_max_f32_e32 v187, v187, v187
	v_max_f32_e32 v186, v186, v187
	v_mul_f32_e32 v195, 0xbe38aa3b, v186
	v_fmamk_f32 v82, v82, 0x3e38aa3b, v195
	v_exp_f32_e32 v82, v82
	v_fmamk_f32 v83, v83, 0x3e38aa3b, v195
	v_exp_f32_e32 v83, v83
	v_fmamk_f32 v84, v84, 0x3e38aa3b, v195
	v_exp_f32_e32 v84, v84
	v_fmamk_f32 v85, v85, 0x3e38aa3b, v195
	v_exp_f32_e32 v85, v85
	v_fmamk_f32 v86, v86, 0x3e38aa3b, v195
	v_add_f32_e32 v186, 0, v82
	v_exp_f32_e32 v86, v86
	v_fmamk_f32 v87, v87, 0x3e38aa3b, v195
	v_add_f32_e32 v186, v186, v83
	v_exp_f32_e32 v87, v87
	v_fmamk_f32 v88, v88, 0x3e38aa3b, v195
	v_add_f32_e32 v186, v186, v84
	v_exp_f32_e32 v88, v88
	v_fmamk_f32 v89, v89, 0x3e38aa3b, v195
	v_add_f32_e32 v186, v186, v85
	v_exp_f32_e32 v89, v89
	v_add_f32_e32 v186, v186, v86
	v_add_f32_e32 v186, v186, v87
	v_add_f32_e32 v186, v186, v88
	v_add_f32_e32 v190, v186, v89
	v_cvt_pk_f16_f32 v186, v82, v83
	v_fmamk_f32 v82, v90, 0x3e38aa3b, v195
	v_exp_f32_e32 v82, v82
	v_fmamk_f32 v83, v91, 0x3e38aa3b, v195
	v_cvt_pk_f16_f32 v187, v84, v85
	v_exp_f32_e32 v83, v83
	v_fmamk_f32 v84, v92, 0x3e38aa3b, v195
	v_exp_f32_e32 v84, v84
	v_fmamk_f32 v85, v93, 0x3e38aa3b, v195
	v_cvt_pk_f16_f32 v188, v86, v87
	v_exp_f32_e32 v85, v85
	v_fmamk_f32 v87, v94, 0x3e38aa3b, v195
	v_cvt_pk_f16_f32 v189, v88, v89
	v_add_f32_e32 v86, v190, v82
	v_exp_f32_e32 v87, v87
	v_fmamk_f32 v88, v95, 0x3e38aa3b, v195
	v_add_f32_e32 v86, v86, v83
	v_exp_f32_e32 v88, v88
	v_fmamk_f32 v89, v96, 0x3e38aa3b, v195
	v_add_f32_e32 v86, v86, v84
	v_exp_f32_e32 v89, v89
	v_fmamk_f32 v90, v97, 0x3e38aa3b, v195
	v_add_f32_e32 v86, v86, v85
	v_exp_f32_e32 v93, v90
	v_fmamk_f32 v66, v66, 0x3e38aa3b, v195
	v_add_f32_e32 v86, v86, v87
	v_exp_f32_e32 v66, v66
	v_fmamk_f32 v67, v67, 0x3e38aa3b, v195
	v_add_f32_e32 v86, v86, v88
	v_exp_f32_e32 v67, v67
	v_fmamk_f32 v68, v68, 0x3e38aa3b, v195
	v_add_f32_e32 v86, v86, v89
	v_exp_f32_e32 v68, v68
	v_fmamk_f32 v69, v69, 0x3e38aa3b, v195
	v_add_f32_e32 v86, v86, v93
	v_exp_f32_e32 v69, v69
	v_fmamk_f32 v70, v70, 0x3e38aa3b, v195
	v_cvt_pk_f16_f32 v90, v82, v83
	v_add_f32_e32 v82, v86, v66
	v_exp_f32_e32 v70, v70
	v_fmamk_f32 v71, v71, 0x3e38aa3b, v195
	v_add_f32_e32 v82, v82, v67
	v_exp_f32_e32 v71, v71
	v_fmamk_f32 v72, v72, 0x3e38aa3b, v195
	v_add_f32_e32 v82, v82, v68
	v_exp_f32_e32 v72, v72
	v_fmamk_f32 v73, v73, 0x3e38aa3b, v195
	v_add_f32_e32 v82, v82, v69
	v_exp_f32_e32 v73, v73
	v_cvt_pk_f16_f32 v190, v66, v67
	v_fmamk_f32 v66, v74, 0x3e38aa3b, v195
	v_add_f32_e32 v82, v82, v70
	v_exp_f32_e32 v66, v66
	v_fmamk_f32 v67, v75, 0x3e38aa3b, v195
	v_add_f32_e32 v82, v82, v71
	v_cvt_pk_f16_f32 v191, v68, v69
	v_exp_f32_e32 v67, v67
	v_fmamk_f32 v68, v76, 0x3e38aa3b, v195
	v_add_f32_e32 v82, v82, v72
	v_exp_f32_e32 v68, v68
	v_fmamk_f32 v69, v77, 0x3e38aa3b, v195
	v_add_f32_e32 v82, v82, v73
	v_cvt_pk_f16_f32 v192, v70, v71
	v_exp_f32_e32 v69, v69
	v_fmamk_f32 v71, v78, 0x3e38aa3b, v195
	v_cvt_pk_f16_f32 v193, v72, v73
	v_add_f32_e32 v70, v82, v66
	v_exp_f32_e32 v71, v71
	v_fmamk_f32 v72, v79, 0x3e38aa3b, v195
	v_add_f32_e32 v70, v70, v67
	v_exp_f32_e32 v72, v72
	v_fmamk_f32 v73, v80, 0x3e38aa3b, v195
	v_add_f32_e32 v70, v70, v68
	v_exp_f32_e32 v73, v73
	v_fmamk_f32 v74, v81, 0x3e38aa3b, v195
	v_add_f32_e32 v70, v70, v69
	v_exp_f32_e32 v74, v74
	v_fmamk_f32 v50, v50, 0x3e38aa3b, v195
	v_add_f32_e32 v70, v70, v71
	v_exp_f32_e32 v50, v50
	v_fmamk_f32 v51, v51, 0x3e38aa3b, v195
	v_add_f32_e32 v70, v70, v72
	v_exp_f32_e32 v51, v51
	v_fmamk_f32 v52, v52, 0x3e38aa3b, v195
	v_add_f32_e32 v70, v70, v73
	v_exp_f32_e32 v52, v52
	v_fmamk_f32 v53, v53, 0x3e38aa3b, v195
	v_add_f32_e32 v70, v70, v74
	v_exp_f32_e32 v53, v53
	v_fmamk_f32 v54, v54, 0x3e38aa3b, v195
	v_cvt_pk_f16_f32 v86, v66, v67
	v_add_f32_e32 v66, v70, v50
	v_exp_f32_e32 v54, v54
	v_fmamk_f32 v55, v55, 0x3e38aa3b, v195
	v_add_f32_e32 v66, v66, v51
	v_exp_f32_e32 v55, v55
	v_fmamk_f32 v56, v56, 0x3e38aa3b, v195
	v_add_f32_e32 v66, v66, v52
	v_exp_f32_e32 v56, v56
	v_fmamk_f32 v57, v57, 0x3e38aa3b, v195
	v_add_f32_e32 v66, v66, v53
	v_exp_f32_e32 v57, v57
	v_cvt_pk_f16_f32 v94, v50, v51
	v_fmamk_f32 v50, v58, 0x3e38aa3b, v195
	v_add_f32_e32 v66, v66, v54
	v_exp_f32_e32 v50, v50
	v_fmamk_f32 v51, v59, 0x3e38aa3b, v195
	v_add_f32_e32 v66, v66, v55
	v_cvt_pk_f16_f32 v95, v52, v53
	v_exp_f32_e32 v51, v51
	v_fmamk_f32 v52, v60, 0x3e38aa3b, v195
	v_add_f32_e32 v66, v66, v56
	v_exp_f32_e32 v52, v52
	v_fmamk_f32 v53, v61, 0x3e38aa3b, v195
	v_add_f32_e32 v66, v66, v57
	v_cvt_pk_f16_f32 v96, v54, v55
	v_exp_f32_e32 v53, v53
	v_fmamk_f32 v55, v62, 0x3e38aa3b, v195
	v_cvt_pk_f16_f32 v97, v56, v57
	v_add_f32_e32 v54, v66, v50
	v_exp_f32_e32 v55, v55
	v_fmamk_f32 v56, v63, 0x3e38aa3b, v195
	v_add_f32_e32 v54, v54, v51
	v_exp_f32_e32 v56, v56
	v_fmamk_f32 v57, v64, 0x3e38aa3b, v195
	v_add_f32_e32 v54, v54, v52
	v_exp_f32_e32 v57, v57
	v_fmamk_f32 v58, v65, 0x3e38aa3b, v195
	v_add_f32_e32 v54, v54, v53
	v_exp_f32_e32 v58, v58
	v_fmamk_f32 v34, v34, 0x3e38aa3b, v195
	v_add_f32_e32 v54, v54, v55
	v_exp_f32_e32 v34, v34
	v_fmamk_f32 v35, v35, 0x3e38aa3b, v195
	v_add_f32_e32 v54, v54, v56
	v_exp_f32_e32 v35, v35
	v_fmamk_f32 v36, v36, 0x3e38aa3b, v195
	v_add_f32_e32 v54, v54, v57
	v_exp_f32_e32 v36, v36
	v_fmamk_f32 v37, v37, 0x3e38aa3b, v195
	v_add_f32_e32 v54, v54, v58
	v_exp_f32_e32 v37, v37
	v_fmamk_f32 v38, v38, 0x3e38aa3b, v195
	v_cvt_pk_f16_f32 v82, v50, v51
	v_add_f32_e32 v50, v54, v34
	v_exp_f32_e32 v38, v38
	v_fmamk_f32 v39, v39, 0x3e38aa3b, v195
	v_add_f32_e32 v50, v50, v35
	v_exp_f32_e32 v39, v39
	v_fmamk_f32 v40, v40, 0x3e38aa3b, v195
	v_add_f32_e32 v50, v50, v36
	v_exp_f32_e32 v40, v40
	v_fmamk_f32 v41, v41, 0x3e38aa3b, v195
	v_add_f32_e32 v50, v50, v37
	v_exp_f32_e32 v51, v41
	v_add_f32_e32 v41, v50, v38
	v_add_f32_e32 v41, v41, v39
	v_add_f32_e32 v41, v41, v40
	v_cvt_pk_f16_f32 v83, v52, v53
	v_add_f32_e32 v41, v41, v51
	v_cvt_pk_f16_f32 v34, v34, v35
	v_cvt_pk_f16_f32 v35, v36, v37
	v_cvt_pk_f16_f32 v37, v40, v51
	ds_read_b128 v[50:53], v219 offset:28224
	v_cvt_pk_f16_f32 v36, v38, v39
	v_fmamk_f32 v38, v42, 0x3e38aa3b, v195
	v_fmamk_f32 v39, v43, 0x3e38aa3b, v195
	v_fmamk_f32 v42, v45, 0x3e38aa3b, v195
	v_exp_f32_e32 v40, v39
	v_fmamk_f32 v39, v44, 0x3e38aa3b, v195
	v_exp_f32_e32 v204, v42
	ds_read_b128 v[42:45], v219 offset:43072
	ds_read_b128 v[196:199], v219 offset:28256
	v_cvt_pk_f16_f32 v92, v87, v88
	v_cvt_pk_f16_f32 v93, v89, v93
	v_cvt_pk_f16_f32 v87, v68, v69
	v_cvt_pk_f16_f32 v88, v71, v72
	v_cvt_pk_f16_f32 v89, v73, v74
	v_exp_f32_e32 v38, v38
	s_waitcnt lgkmcnt(2)
	v_mfma_f32_32x32x16_f16 v[66:81], v[50:53], v[186:189], 0
	ds_read_b128 v[200:203], v219 offset:43104
	v_cvt_pk_f16_f32 v91, v84, v85
	v_cvt_pk_f16_f32 v84, v55, v56
	v_cvt_pk_f16_f32 v85, v57, v58
	v_exp_f32_e32 v39, v39
	v_fmamk_f32 v46, v46, 0x3e38aa3b, v195
	v_add_f32_e32 v41, v41, v38
	s_waitcnt lgkmcnt(2)
	v_mfma_f32_32x32x16_f16 v[50:65], v[42:45], v[186:189], 0
	v_exp_f32_e32 v46, v46
	v_fmamk_f32 v47, v47, 0x3e38aa3b, v195
	v_add_f32_e32 v41, v41, v40
	v_exp_f32_e32 v47, v47
	v_fmamk_f32 v48, v48, 0x3e38aa3b, v195
	v_add_f32_e32 v41, v41, v39
	v_exp_f32_e32 v48, v48
	v_fmamk_f32 v42, v49, 0x3e38aa3b, v195
	v_add_f32_e32 v41, v41, v204
	v_exp_f32_e32 v49, v42
	v_fmamk_f32 v18, v18, 0x3e38aa3b, v195
	ds_read_b128 v[42:45], v219 offset:28288
	v_add_f32_e32 v41, v41, v46
	s_waitcnt lgkmcnt(2)
	v_mfma_f32_32x32x16_f16 v[66:81], v[196:199], v[90:93], v[66:81]
	v_exp_f32_e32 v18, v18
	v_fmamk_f32 v19, v19, 0x3e38aa3b, v195
	v_add_f32_e32 v41, v41, v47
	v_exp_f32_e32 v19, v19
	v_add_f32_e32 v41, v41, v48
	v_add_f32_e32 v186, v41, v49
	v_fmamk_f32 v20, v20, 0x3e38aa3b, v195
	s_waitcnt lgkmcnt(1)
	v_mfma_f32_32x32x16_f16 v[50:65], v[200:203], v[90:93], v[50:65]
	v_cvt_pk_f16_f32 v38, v38, v40
	v_cvt_pk_f16_f32 v40, v46, v47
	v_add_f32_e32 v46, v186, v18
	v_exp_f32_e32 v20, v20
	v_cvt_pk_f16_f32 v41, v48, v49
	v_add_f32_e32 v186, v46, v19
	ds_read_b128 v[46:49], v219 offset:43136
	ds_read_b128 v[90:93], v219 offset:28320
	v_fmamk_f32 v21, v21, 0x3e38aa3b, v195
	v_exp_f32_e32 v21, v21
	v_fmamk_f32 v22, v22, 0x3e38aa3b, v195
	s_waitcnt lgkmcnt(2)
	v_mfma_f32_32x32x16_f16 v[66:81], v[42:45], v[190:193], v[66:81]
	v_add_f32_e32 v42, v186, v20
	v_exp_f32_e32 v186, v22
	v_fmamk_f32 v23, v23, 0x3e38aa3b, v195
	v_add_f32_e32 v22, v42, v21
	ds_read_b128 v[42:45], v219 offset:43168
	v_add_f32_e32 v22, v22, v186
	v_cvt_pk_f16_f32 v18, v18, v19
	s_waitcnt lgkmcnt(2)
	v_mfma_f32_32x32x16_f16 v[50:65], v[46:49], v[190:193], v[50:65]
	v_exp_f32_e32 v46, v23
	v_fmamk_f32 v23, v24, 0x3e38aa3b, v195
	v_exp_f32_e32 v47, v23
	v_fmamk_f32 v23, v25, 0x3e38aa3b, v195
	v_exp_f32_e32 v48, v23
	v_add_f32_e32 v22, v22, v46
	v_add_f32_e32 v22, v22, v47
	s_waitcnt lgkmcnt(1)
	v_mfma_f32_32x32x16_f16 v[66:81], v[90:93], v[86:89], v[66:81]
	v_add_f32_e32 v49, v22, v48
	ds_read_b128 v[22:25], v219 offset:28352
	v_fmamk_f32 v19, v26, 0x3e38aa3b, v195
	v_exp_f32_e32 v90, v19
	v_cvt_pk_f16_f32 v19, v20, v21
	v_cvt_pk_f16_f32 v20, v186, v46
	v_cvt_pk_f16_f32 v21, v47, v48
	s_waitcnt lgkmcnt(1)
	v_mfma_f32_32x32x16_f16 v[50:65], v[42:45], v[86:89], v[50:65]
	v_add_f32_e32 v26, v49, v90
	ds_read_b128 v[42:45], v219 offset:43200
	ds_read_b128 v[46:49], v219 offset:28384
	v_fmamk_f32 v27, v27, 0x3e38aa3b, v195
	v_exp_f32_e32 v86, v27
	v_fmamk_f32 v27, v30, 0x3e38aa3b, v195
	v_exp_f32_e32 v30, v27
	v_fmamk_f32 v27, v31, 0x3e38aa3b, v195
	s_waitcnt lgkmcnt(2)
	v_mfma_f32_32x32x16_f16 v[66:81], v[22:25], v[94:97], v[66:81]
	v_fmamk_f32 v22, v28, 0x3e38aa3b, v195
	v_exp_f32_e32 v87, v22
	v_fmamk_f32 v22, v29, 0x3e38aa3b, v195
	v_exp_f32_e32 v88, v22
	ds_read_b128 v[22:25], v219 offset:43232
	v_add_f32_e32 v26, v26, v86
	v_exp_f32_e32 v31, v27
	s_waitcnt lgkmcnt(2)
	v_mfma_f32_32x32x16_f16 v[50:65], v[42:45], v[94:97], v[50:65]
	v_fmamk_f32 v27, v32, 0x3e38aa3b, v195
	v_add_f32_e32 v26, v26, v87
	v_exp_f32_e32 v32, v27
	v_add_f32_e32 v26, v26, v88
	v_add_f32_e32 v26, v26, v30
	v_add_f32_e32 v26, v26, v31
	v_fmamk_f32 v27, v33, 0x3e38aa3b, v195
	v_exp_f32_e32 v33, v27
	v_add_f32_e32 v42, v26, v32
	ds_read_b128 v[26:29], v219 offset:28416
	s_waitcnt lgkmcnt(2)
	v_mfma_f32_32x32x16_f16 v[66:81], v[46:49], v[82:85], v[66:81]
	v_add_f32_e32 v46, v42, v33
	v_fmamk_f32 v2, v2, 0x3e38aa3b, v195
	v_exp_f32_e32 v47, v2
	v_fmamk_f32 v2, v3, 0x3e38aa3b, v195
	v_exp_f32_e32 v48, v2
	v_fmamk_f32 v2, v4, 0x3e38aa3b, v195
	v_exp_f32_e32 v49, v2
	s_waitcnt lgkmcnt(1)
	v_mfma_f32_32x32x16_f16 v[50:65], v[22:25], v[82:85], v[50:65]
	v_cvt_pk_f16_f32 v24, v30, v31
	v_cvt_pk_f16_f32 v25, v32, v33
	ds_read_b128 v[30:33], v219 offset:43264
	ds_read_b128 v[42:45], v219 offset:28448
	v_fmamk_f32 v2, v5, 0x3e38aa3b, v195
	v_cvt_pk_f16_f32 v39, v39, v204
	v_cvt_pk_f16_f32 v22, v90, v86
	v_cvt_pk_f16_f32 v23, v87, v88
	s_waitcnt lgkmcnt(2)
	v_mfma_f32_32x32x16_f16 v[66:81], v[26:29], v[34:37], v[66:81]
	ds_read_b128 v[26:29], v219 offset:43296
	s_waitcnt lgkmcnt(2)
	v_mfma_f32_32x32x16_f16 v[50:65], v[30:33], v[34:37], v[50:65]
	v_exp_f32_e32 v30, v2
	v_add_f32_e32 v2, v46, v47
	v_add_f32_e32 v2, v2, v48
	v_add_f32_e32 v2, v2, v49
	v_add_f32_e32 v31, v2, v30
	v_fmamk_f32 v2, v6, 0x3e38aa3b, v195
	v_exp_f32_e32 v32, v2
	v_fmamk_f32 v2, v7, 0x3e38aa3b, v195
	v_exp_f32_e32 v33, v2
	v_fmamk_f32 v2, v8, 0x3e38aa3b, v195
	v_exp_f32_e32 v34, v2
	ds_read_b128 v[2:5], v219 offset:28480
	s_waitcnt lgkmcnt(2)
	v_mfma_f32_32x32x16_f16 v[66:81], v[42:45], v[38:41], v[66:81]
	v_fmamk_f32 v6, v9, 0x3e38aa3b, v195
	v_exp_f32_e32 v35, v6
	v_add_f32_e32 v6, v31, v32
	v_add_f32_e32 v6, v6, v33
	v_add_f32_e32 v6, v6, v34
	v_add_f32_e32 v36, v6, v35
	s_waitcnt lgkmcnt(1)
	v_mfma_f32_32x32x16_f16 v[50:65], v[26:29], v[38:41], v[50:65]
	ds_read_b128 v[6:9], v219 offset:43328
	ds_read_b128 v[26:29], v219 offset:28512
	s_waitcnt lgkmcnt(2)
	v_mfma_f32_32x32x16_f16 v[66:81], v[2:5], v[18:21], v[66:81]
	v_fmamk_f32 v5, v10, 0x3e38aa3b, v195
	v_exp_f32_e32 v37, v5
	v_cvt_pk_f16_f32 v5, v34, v35
	v_cvt_pk_f16_f32 v3, v49, v30
	v_cvt_pk_f16_f32 v4, v32, v33
	ds_read_b128 v[30:33], v219 offset:43360
	v_fmamk_f32 v10, v15, 0x3e38aa3b, v195
	s_waitcnt lgkmcnt(2)
	v_mfma_f32_32x32x16_f16 v[50:65], v[6:9], v[18:21], v[50:65]
	v_fmamk_f32 v7, v11, 0x3e38aa3b, v195
	v_exp_f32_e32 v18, v7
	v_fmamk_f32 v7, v12, 0x3e38aa3b, v195
	v_exp_f32_e32 v34, v7
	v_fmamk_f32 v7, v13, 0x3e38aa3b, v195
	v_exp_f32_e32 v35, v7
	v_add_f32_e32 v6, v36, v37
	v_add_f32_e32 v6, v6, v18
	v_add_f32_e32 v6, v6, v34
	v_add_f32_e32 v19, v6, v35
	v_fmamk_f32 v6, v14, 0x3e38aa3b, v195
	s_waitcnt lgkmcnt(1)
	v_mfma_f32_32x32x16_f16 v[66:81], v[26:29], v[22:25], v[66:81]
	v_exp_f32_e32 v26, v6
	ds_read_b128 v[6:9], v219 offset:28544
	v_cvt_pk_f16_f32 v2, v47, v48
	s_waitcnt lgkmcnt(1)
	v_mfma_f32_32x32x16_f16 v[50:65], v[30:33], v[22:25], v[50:65]
	v_exp_f32_e32 v22, v10
	v_fmamk_f32 v10, v16, 0x3e38aa3b, v195
	v_exp_f32_e32 v23, v10
	v_fmamk_f32 v10, v17, 0x3e38aa3b, v195
	v_exp_f32_e32 v24, v10
	ds_read_b128 v[10:13], v219 offset:43392
	ds_read_b128 v[14:17], v219 offset:28576
	s_waitcnt lgkmcnt(2)
	v_mfma_f32_32x32x16_f16 v[66:81], v[6:9], v[2:5], v[66:81]
	v_add_f32_e32 v6, v19, v26
	v_add_f32_e32 v6, v6, v22
	v_add_f32_e32 v6, v6, v23
	v_add_f32_e32 v25, v6, v24
	v_cvt_pk_f16_f32 v6, v37, v18
	ds_read_b128 v[18:21], v219 offset:43424
	v_fmamk_f32 v7, v230, 0x3e38aa3b, v195
	s_waitcnt lgkmcnt(2)
	v_mfma_f32_32x32x16_f16 v[50:65], v[10:13], v[2:5], v[50:65]
	v_fmamk_f32 v2, v229, 0x3e38aa3b, v195
	v_exp_f32_e32 v12, v2
	v_fmamk_f32 v2, v228, 0x3e38aa3b, v195
	v_cvt_pk_f16_f32 v8, v26, v22
	v_exp_f32_e32 v22, v2
	v_fmamk_f32 v2, v227, 0x3e38aa3b, v195
	v_exp_f32_e32 v10, v7
	v_cvt_pk_f16_f32 v7, v34, v35
	v_cvt_pk_f16_f32 v9, v23, v24
	v_exp_f32_e32 v23, v2
	ds_read_b128 v[2:5], v219 offset:28608
	s_waitcnt lgkmcnt(2)
	v_mfma_f32_32x32x16_f16 v[66:81], v[14:17], v[6:9], v[66:81]
	v_fmac_f32_e32 v195, 0xf149f2ca, v224
	v_exp_f32_e32 v24, v195
	v_add_f32_e32 v11, v25, v10
	s_waitcnt lgkmcnt(1)
	v_mfma_f32_32x32x16_f16 v[50:65], v[18:21], v[6:9], v[50:65]
	v_cvt_pk_f16_f32 v8, v24, v24
	v_add_f32_e32 v18, v11, v12
	v_cvt_pk_f16_f32 v6, v10, v12
	v_cvt_pk_f16_f32 v7, v22, v23
	v_mov_b32_e32 v9, v8
	ds_read_b128 v[10:13], v219 offset:43456
	ds_read_b128 v[14:17], v219 offset:28640
	s_waitcnt lgkmcnt(2)
	v_mfma_f32_32x32x16_f16 v[66:81], v[2:5], v[6:9], v[66:81]
	v_add_f32_e32 v2, v18, v22
	v_add_f32_e32 v2, v2, v23
	v_add_f32_e32 v2, v2, v24
	ds_read_b128 v[18:21], v219 offset:43488
	v_add_f32_e32 v2, v2, v24
	v_add_f32_e32 v2, v2, v24
	v_add_f32_e32 v2, v2, v24
	s_waitcnt lgkmcnt(2)
	v_mfma_f32_32x32x16_f16 v[50:65], v[10:13], v[6:9], v[50:65]
	v_add_f32_e32 v2, v2, v24
	v_add_f32_e32 v2, v2, v24
	v_add_f32_e32 v2, v2, v24
	v_add_f32_e32 v2, v2, v24
	v_mov_b32_e32 v4, v8
	v_mov_b32_e32 v5, v8
	v_mov_b32_e32 v6, v8
	v_mov_b32_e32 v7, v8
	v_add_f32_e32 v2, v2, v24
	v_add_f32_e32 v2, v2, v24
	s_waitcnt lgkmcnt(1)
	v_mfma_f32_32x32x16_f16 v[66:81], v[14:17], v[4:7], v[66:81]
	v_add_f32_e32 v2, v2, v24
	v_add_f32_e32 v2, v2, v24
	ds_bpermute_b32 v3, v194, v2
	s_waitcnt lgkmcnt(1)
	v_mfma_f32_32x32x16_f16 v[50:65], v[18:21], v[4:7], v[50:65]
	s_and_saveexec_b64 s[10:11], vcc
	s_cbranch_execz .LBB2_23
	s_waitcnt lgkmcnt(0)
	v_add_f32_e32 v2, v2, v3
	v_div_scale_f32 v3, s[20:21], v2, v2, 1.0
	v_rcp_f32_e32 v4, v3
	v_div_scale_f32 v5, vcc, 1.0, v2, 1.0
	v_fma_f32 v6, -v3, v4, 1.0
	v_fmac_f32_e32 v4, v6, v4
	v_mul_f32_e32 v6, v5, v4
	v_fma_f32 v7, -v3, v6, v5
	v_fmac_f32_e32 v6, v7, v4
	v_fma_f32 v3, -v3, v6, v5
	v_div_fmas_f32 v3, v3, v4, v6
	v_div_fixup_f32 v2, v3, v2, 1.0
	v_add_lshl_u32 v3, v225, s16, 6
	v_add3_u32 v3, s15, v3, v226
	v_mad_i64_i32 v[4:5], s[20:21], v3, s18, v[210:211]
	v_mbcnt_lo_u32_b32 v22, -1, 0
	v_mbcnt_hi_u32_b32 v22, -1, v22
	v_and_b32_e32 v22, 32, v22
	v_lshrrev_b32_e32 v22, 2, v22
	v_mov_b32_e32 v23, 0
	v_lshl_add_u64 v[4:5], v[22:23], 0, v[4:5]
	v_pk_mul_f32 v[6:7], v[2:3], v[66:67] op_sel_hi:[0,1]
	v_pk_mul_f32 v[8:9], v[2:3], v[68:69] op_sel_hi:[0,1]
	v_cvt_pk_f16_f32 v10, v6, v7
	v_cvt_pk_f16_f32 v11, v8, v9
	v_pk_mul_f32 v[6:7], v[2:3], v[70:71] op_sel_hi:[0,1]
	v_pk_mul_f32 v[8:9], v[2:3], v[72:73] op_sel_hi:[0,1]
	v_cvt_pk_f16_f32 v12, v6, v7
	v_cvt_pk_f16_f32 v13, v8, v9
	s_nop 1
	v_permlane32_swap_b32_e32 v10, v12
	v_permlane32_swap_b32_e32 v11, v13
	global_store_dwordx4 v[4:5], v[10:13], off
	v_pk_mul_f32 v[6:7], v[2:3], v[50:51] op_sel_hi:[0,1]
	v_pk_mul_f32 v[8:9], v[2:3], v[52:53] op_sel_hi:[0,1]
	v_cvt_pk_f16_f32 v14, v6, v7
	v_cvt_pk_f16_f32 v15, v8, v9
	v_pk_mul_f32 v[6:7], v[2:3], v[54:55] op_sel_hi:[0,1]
	v_pk_mul_f32 v[8:9], v[2:3], v[56:57] op_sel_hi:[0,1]
	v_cvt_pk_f16_f32 v16, v6, v7
	v_cvt_pk_f16_f32 v17, v8, v9
	s_nop 1
	v_permlane32_swap_b32_e32 v14, v16
	v_permlane32_swap_b32_e32 v15, v17
	global_store_dwordx4 v[4:5], v[14:17], off offset:64
	v_pk_mul_f32 v[6:7], v[2:3], v[74:75] op_sel_hi:[0,1]
	v_pk_mul_f32 v[8:9], v[2:3], v[76:77] op_sel_hi:[0,1]
	v_cvt_pk_f16_f32 v18, v6, v7
	v_cvt_pk_f16_f32 v19, v8, v9
	v_pk_mul_f32 v[6:7], v[2:3], v[78:79] op_sel_hi:[0,1]
	v_pk_mul_f32 v[8:9], v[2:3], v[80:81] op_sel_hi:[0,1]
	v_cvt_pk_f16_f32 v20, v6, v7
	v_cvt_pk_f16_f32 v21, v8, v9
	s_nop 1
	v_permlane32_swap_b32_e32 v18, v20
	v_permlane32_swap_b32_e32 v19, v21
	global_store_dwordx4 v[4:5], v[18:21], off offset:32
	v_pk_mul_f32 v[6:7], v[2:3], v[58:59] op_sel_hi:[0,1]
	v_pk_mul_f32 v[8:9], v[2:3], v[60:61] op_sel_hi:[0,1]
	v_cvt_pk_f16_f32 v10, v6, v7
	v_cvt_pk_f16_f32 v11, v8, v9
	v_pk_mul_f32 v[6:7], v[2:3], v[62:63] op_sel_hi:[0,1]
	v_pk_mul_f32 v[8:9], v[2:3], v[64:65] op_sel_hi:[0,1]
	v_cvt_pk_f16_f32 v12, v6, v7
	v_cvt_pk_f16_f32 v13, v8, v9
	s_nop 1
	v_permlane32_swap_b32_e32 v10, v12
	v_permlane32_swap_b32_e32 v11, v13
	global_store_dwordx4 v[4:5], v[10:13], off offset:96
	s_branch .LBB2_23
